# late weight conversion of P1 rewritten by hand (LDS-DMA loads, 2 items in flight per wave, swizzled LDS transpose); even workgroups convert before the GEMMs, odd after
# baseline (speedup 1.0000x reference)
; #define LAS __attribute__((address_space(3)))
; template <bool NT = false> __device__ __forceinline__ void conv_item(const float* W, int K, int Nsrc, int nblk, bf16* WT, LAS float* scr, int item, int lane) {
;     const int kb = item / nblk, nb = item - kb * nblk, k0 = 64 * kb, n0 = 32 * nb;
;     const int nl = n0 + (lane & 31); const bool ok = nl < Nsrc; const int nlc = ok ? nl : Nsrc - 1;
;     float wv_[32];
; #pragma unroll
;     for (int i = 0; i < 32; ++i) { const int kk = 2 * i + (lane >> 5); wv_[i] = __builtin_nontemporal_load(W + (size_t)(k0 + kk) * Nsrc + nlc); }
; template <int PART> __device__ __forceinline__ void convert_weights(Frame& F, int l, int wg_lo) {
;     ...
;         const int cw = (int)blockIdx.x; int nsl, s0; if (cw < 160) { nsl = 3; s0 = 3 * cw; } else { nsl = 2; s0 = 480 + 2 * (cw - 160); }
;         (void)wg_lo;
;         for (int sl = s0; sl < s0 + nsl; ++sl)
;         for (int it = sl * NWAVES + F.wave; it < I4 + I5 + I6; it += 672 * NWAVES) {
;             int r = it;
;             if (r < I4) { conv_item<true>(F.w_out + (size_t)l * D * D, D, D, 64, F.Wout, scr, r, lane); continue; } r -= I4;
;             if (r < I5) { conv_item<true>(F.w_up + (size_t)l * D * FF, D, FF, 256, F.Wup, scr, r, lane); continue; } r -= I5;
;             conv_item<true>(F.w_down + (size_t)l * FF * D, FF, D, 64, F.Wdown, scr, r, lane);
;         }
.LBB0_174:
	s_cmp_eq_u32 s100, 2
	s_cbranch_scc1 .Lp1_conv_skip
	v_mbcnt_lo_u32_b32 v0, -1, 0
	v_mbcnt_hi_u32_b32 v0, -1, v0
	s_lshl_b64 s[4:5], s[16:17], 26
	s_lshl_b64 s[6:7], s[16:17], 24
	v_readlane_b32 s0, v251, 2
	v_readlane_b32 s1, v251, 3
	v_lshrrev_b32_e32 v1, 3, v0
	v_and_b32_e32 v2, 7, v0
	s_add_u32 s2, s0, s4
	s_addc_u32 s3, s1, s5
	v_readlane_b32 s0, v251, 12
	v_readlane_b32 s1, v251, 13
	v_lshrrev_b32_e32 v3, 5, v0
	v_and_b32_e32 v9, 3, v1
	s_add_u32 s4, s0, s4
	s_addc_u32 s5, s1, s5
	v_readlane_b32 s0, v251, 10
	v_readlane_b32 s1, v251, 11
	v_xor_b32_e32 v8, v2, v3
	v_lshlrev_b32_e32 v10, 10, v2
	s_add_u32 s6, s0, s6
	s_addc_u32 s7, s1, s7
	v_lshl_add_u32 v10, v9, 2, v10
	v_lshlrev_b32_e32 v19, 4, v2
	v_xor_b32_e32 v4, 0, v8
	v_xor_b32_e32 v5, 2, v8
	v_xor_b32_e32 v6, 4, v8
	v_xor_b32_e32 v7, 6, v8
	v_lshl_add_u32 v4, v4, 4, v10
	v_lshl_add_u32 v5, v5, 4, v10
	v_lshl_add_u32 v6, v6, 4, v10
	v_lshl_add_u32 v7, v7, 4, v10
	s_lshl_b32 s19, s35, 14
	v_readlane_b32 s20, v255, 12
	s_nop 0
	s_lshl_b32 s0, s20, 1
	s_add_i32 s0, s0, 0xa0
	s_mul_i32 s10, s20, 3
	s_cmpk_lt_u32 s20, 0xa0
	s_cselect_b32 s10, s10, s0
	s_cselect_b32 s11, 12, 8
	s_mov_b32 s12, -1
	s_mov_b32 s62, 0
.Lcw1_adv_p:
	s_add_i32 s12, s12, 1
	s_cmp_ge_u32 s12, s11
	s_cbranch_scc1 .Lcw1_end
	s_lshr_b32 s0, s12, 2
	s_add_i32 s0, s0, s10
	s_lshl_b32 s0, s0, 3
	s_add_i32 s0, s0, s35
	s_and_b32 s1, s12, 3
	s_mulk_i32 s1, 0x1500
	s_add_i32 s0, s0, s1
	s_cmpk_ge_u32 s0, 0x4800
	s_cbranch_scc1 .Lcw1_adv_p
	s_cmpk_lt_u32 s0, 0x800
	s_cbranch_scc1 .Lcw1_wo_p
	s_cmpk_lt_u32 s0, 0x2800
	s_cbranch_scc1 .Lcw1_wu_p
	s_sub_u32 s0, s0, 0x2800
	s_lshr_b32 s1, s0, 6
	s_and_b32 s0, s0, 63
	s_lshl_b32 s13, s1, 19
	s_lshl_b32 s20, s0, 7
	s_add_u32 s13, s13, s20
	s_add_u32 s14, s2, s13
	s_addc_u32 s15, s3, 0
	s_lshl_b32 s0, s0, 19
	s_lshl_b32 s1, s1, 7
	s_add_u32 s0, s0, s1
	s_add_u32 s0, s0, 0x6900000
	s_movk_i32 s13, 0x2000
	s_movk_i32 s8, 0x4000
	s_branch .Lcw1_dec_p
.Lcw1_wo_p:
	s_lshr_b32 s1, s0, 6
	s_and_b32 s0, s0, 63
	s_lshl_b32 s13, s1, 19
	s_lshl_b32 s20, s0, 7
	s_add_u32 s13, s13, s20
	s_add_u32 s14, s6, s13
	s_addc_u32 s15, s7, 0
	s_lshl_b32 s0, s0, 17
	s_lshl_b32 s1, s1, 7
	s_add_u32 s0, s0, s1
	s_add_u32 s0, s0, 0x4100000
	s_movk_i32 s13, 0x2000
	s_movk_i32 s8, 0x1000
	s_branch .Lcw1_dec_p
.Lcw1_wu_p:
	s_sub_u32 s0, s0, 0x800
	s_lshr_b32 s1, s0, 8
	s_and_b32 s0, s0, 0xff
	s_lshl_b32 s13, s1, 21
	s_lshl_b32 s20, s0, 7
	s_add_u32 s13, s13, s20
	s_add_u32 s14, s4, s13
	s_addc_u32 s15, s5, 0
	s_lshl_b32 s0, s0, 17
	s_lshl_b32 s1, s1, 7
	s_add_u32 s0, s0, s1
	s_add_u32 s0, s0, 0x4900000
	s_mov_b32 s13, 0x8000
	s_movk_i32 s8, 0x1000
.Lcw1_dec_p:
	v_readlane_b32 s20, v251, 32
	v_readlane_b32 s21, v251, 33
	v_mul_u32_u24_e32 v11, s13, v1
	s_nop 0
	s_add_u32 vcc_lo, s20, s0
	s_addc_u32 vcc_hi, s21, 0
	s_mov_b32 s20, s19
	s_lshl_b32 s21, s13, 3
	v_xor_b32_e32 v12, 0, v2
	s_add_i32 m0, s20, 0x0
	v_lshl_add_u32 v12, v12, 4, v11
	global_load_lds_dwordx4 v12, s[14:15] nt
	s_add_u32 s14, s14, s21
	s_addc_u32 s15, s15, 0
	v_xor_b32_e32 v13, 1, v2
	s_add_i32 m0, s20, 0x400
	v_lshl_add_u32 v13, v13, 4, v11
	global_load_lds_dwordx4 v13, s[14:15] nt
	s_add_u32 s14, s14, s21
	s_addc_u32 s15, s15, 0
	v_xor_b32_e32 v12, 2, v2
	s_add_i32 m0, s20, 0x800
	v_lshl_add_u32 v12, v12, 4, v11
	global_load_lds_dwordx4 v12, s[14:15] nt
	s_add_u32 s14, s14, s21
	s_addc_u32 s15, s15, 0
	v_xor_b32_e32 v13, 3, v2
	s_add_i32 m0, s20, 0xc00
	v_lshl_add_u32 v13, v13, 4, v11
	global_load_lds_dwordx4 v13, s[14:15] nt
	s_add_u32 s14, s14, s21
	s_addc_u32 s15, s15, 0
	v_xor_b32_e32 v12, 4, v2
	s_add_i32 m0, s20, 0x1000
	v_lshl_add_u32 v12, v12, 4, v11
	global_load_lds_dwordx4 v12, s[14:15] nt
	s_add_u32 s14, s14, s21
	s_addc_u32 s15, s15, 0
	v_xor_b32_e32 v13, 5, v2
	s_add_i32 m0, s20, 0x1400
	v_lshl_add_u32 v13, v13, 4, v11
	global_load_lds_dwordx4 v13, s[14:15] nt
	s_add_u32 s14, s14, s21
	s_addc_u32 s15, s15, 0
	v_xor_b32_e32 v12, 6, v2
	s_add_i32 m0, s20, 0x1800
	v_lshl_add_u32 v12, v12, 4, v11
	global_load_lds_dwordx4 v12, s[14:15] nt
	s_add_u32 s14, s14, s21
	s_addc_u32 s15, s15, 0
	v_xor_b32_e32 v13, 7, v2
	s_add_i32 m0, s20, 0x1c00
	v_lshl_add_u32 v13, v13, 4, v11
	global_load_lds_dwordx4 v13, s[14:15] nt
.Lcw1_loop:
	s_mov_b64 s[16:17], vcc
	s_mov_b32 s18, s8

; #define GAS __attribute__((address_space(1)))
; #define LAS __attribute__((address_space(3)))
; #define LDS_WAIT() asm volatile("s_waitcnt lgkmcnt(0)" ::: "memory")
; __device__ __forceinline__ unsigned pk2(float lo, float hi) { return pg8::cvt_pk_bf16(lo, hi); }
; template <bool NT = false> __device__ __forceinline__ void conv_item(const float* W, int K, int Nsrc, int nblk, bf16* WT, LAS float* scr, int item, int lane) {
;     const int kb = item / nblk, nb = item - kb * nblk, k0 = 64 * kb, n0 = 32 * nb;
;     const int nl = n0 + (lane & 31); const bool ok = nl < Nsrc; const int nlc = ok ? nl : Nsrc - 1;
;     float wv_[32];
; #pragma unroll
;     for (int i = 0; i < 32; ++i) { const int kk = 2 * i + (lane >> 5); wv_[i] = __builtin_nontemporal_load(W + (size_t)(k0 + kk) * Nsrc + nlc); }
; #pragma unroll
;     for (int i = 0; i < 32; ++i) { const int kk = 2 * i + (lane >> 5); scr[kk * 33 + (lane & 31)] = ok ? wv_[i] : 0.f; }
;     LDS_WAIT(); asm volatile("" ::: "memory");
;     const int c = lane & 7;
; #pragma unroll
;     for (int j = 0; j < 4; ++j) { const int n = (lane >> 3) + 8 * j; const LAS float* s = scr + (8 * c) * 33 + n;
;         v4u o; o.x = pk2(s[0 * 33], s[1 * 33]); o.y = pk2(s[2 * 33], s[3 * 33]); o.z = pk2(s[4 * 33], s[5 * 33]); o.w = pk2(s[6 * 33], s[7 * 33]);
;         if (NT) __builtin_nontemporal_store(o, (v4u*)(WT + (size_t)(n0 + n) * K + k0 + 8 * c)); else *(GAS v4u*)(WT + (size_t)(n0 + n) * K + k0 + 8 * c) = o; }
;     LDS_WAIT(); asm volatile("" ::: "memory");
; }
.Lcw1_dec_n:
	v_readlane_b32 s20, v251, 32
	v_readlane_b32 s21, v251, 33
	v_mul_u32_u24_e32 v11, s13, v1
	s_nop 0
	s_add_u32 vcc_lo, s20, s0
	s_addc_u32 vcc_hi, s21, 0
	s_xor_b32 s20, s62, 0x2000
	s_add_i32 s20, s20, s19
	s_lshl_b32 s21, s13, 3
	v_xor_b32_e32 v12, 0, v2
	s_add_i32 m0, s20, 0x0
	v_lshl_add_u32 v12, v12, 4, v11
	global_load_lds_dwordx4 v12, s[14:15] nt
	s_add_u32 s14, s14, s21
	s_addc_u32 s15, s15, 0
	v_xor_b32_e32 v13, 1, v2
	s_add_i32 m0, s20, 0x400
	v_lshl_add_u32 v13, v13, 4, v11
	global_load_lds_dwordx4 v13, s[14:15] nt
	s_add_u32 s14, s14, s21
	s_addc_u32 s15, s15, 0
	v_xor_b32_e32 v12, 2, v2
	s_add_i32 m0, s20, 0x800
	v_lshl_add_u32 v12, v12, 4, v11
	global_load_lds_dwordx4 v12, s[14:15] nt
	s_add_u32 s14, s14, s21
	s_addc_u32 s15, s15, 0
	v_xor_b32_e32 v13, 3, v2
	s_add_i32 m0, s20, 0xc00
	v_lshl_add_u32 v13, v13, 4, v11
	global_load_lds_dwordx4 v13, s[14:15] nt
	s_add_u32 s14, s14, s21
	s_addc_u32 s15, s15, 0
	v_xor_b32_e32 v12, 4, v2
	s_add_i32 m0, s20, 0x1000
	v_lshl_add_u32 v12, v12, 4, v11
	global_load_lds_dwordx4 v12, s[14:15] nt
	s_add_u32 s14, s14, s21
	s_addc_u32 s15, s15, 0
	v_xor_b32_e32 v13, 5, v2
	s_add_i32 m0, s20, 0x1400
	v_lshl_add_u32 v13, v13, 4, v11
	global_load_lds_dwordx4 v13, s[14:15] nt
	s_add_u32 s14, s14, s21
	s_addc_u32 s15, s15, 0
	v_xor_b32_e32 v12, 6, v2
	s_add_i32 m0, s20, 0x1800
	v_lshl_add_u32 v12, v12, 4, v11
	global_load_lds_dwordx4 v12, s[14:15] nt
	s_add_u32 s14, s14, s21
	s_addc_u32 s15, s15, 0
	v_xor_b32_e32 v13, 7, v2
	s_add_i32 m0, s20, 0x1c00
	v_lshl_add_u32 v13, v13, 4, v11
	global_load_lds_dwordx4 v13, s[14:15] nt
	s_waitcnt vmcnt(8)
	s_add_i32 s0, s19, s62
	v_add_u32_e32 v14, s0, v4
	v_add_u32_e32 v15, s0, v5
	v_add_u32_e32 v16, s0, v6
	v_add_u32_e32 v17, s0, v7
	ds_read2_b32 v[20:21], v14 offset0:0 offset1:32
	ds_read2_b32 v[22:23], v14 offset0:64 offset1:96
	ds_read2_b32 v[24:25], v14 offset0:128 offset1:160
	ds_read2_b32 v[26:27], v14 offset0:192 offset1:224
	ds_read2_b32 v[28:29], v15 offset0:0 offset1:32
	ds_read2_b32 v[30:31], v15 offset0:64 offset1:96
	ds_read2_b32 v[32:33], v15 offset0:128 offset1:160
	ds_read2_b32 v[34:35], v15 offset0:192 offset1:224
	ds_read2_b32 v[36:37], v16 offset0:0 offset1:32
	ds_read2_b32 v[38:39], v16 offset0:64 offset1:96
	ds_read2_b32 v[40:41], v16 offset0:128 offset1:160
	ds_read2_b32 v[42:43], v16 offset0:192 offset1:224
	ds_read2_b32 v[44:45], v17 offset0:0 offset1:32
	ds_read2_b32 v[46:47], v17 offset0:64 offset1:96
	ds_read2_b32 v[48:49], v17 offset0:128 offset1:160
	ds_read2_b32 v[50:51], v17 offset0:192 offset1:224
	v_mad_u32_u24 v18, v1, s18, v19
	s_lshl_b32 s1, s18, 3
	s_waitcnt lgkmcnt(12)
	v_cvt_pk_bf16_f32 v52, v20, v21
	v_cvt_pk_bf16_f32 v53, v22, v23
	v_cvt_pk_bf16_f32 v54, v24, v25
	v_cvt_pk_bf16_f32 v55, v26, v27
	global_store_dwordx4 v18, v[52:55], s[16:17] nt
	s_add_u32 s16, s16, s1
	s_addc_u32 s17, s17, 0
	s_waitcnt lgkmcnt(8)
	v_cvt_pk_bf16_f32 v56, v28, v29
	v_cvt_pk_bf16_f32 v57, v30, v31
	v_cvt_pk_bf16_f32 v58, v32, v33
	v_cvt_pk_bf16_f32 v59, v34, v35
	global_store_dwordx4 v18, v[56:59], s[16:17] nt
	s_add_u32 s16, s16, s1
	s_addc_u32 s17, s17, 0
	s_waitcnt lgkmcnt(4)
	v_cvt_pk_bf16_f32 v60, v36, v37
	v_cvt_pk_bf16_f32 v61, v38, v39
	v_cvt_pk_bf16_f32 v62, v40, v41
	v_cvt_pk_bf16_f32 v63, v42, v43
	global_store_dwordx4 v18, v[60:63], s[16:17] nt
	s_add_u32 s16, s16, s1
	s_addc_u32 s17, s17, 0
	s_waitcnt lgkmcnt(0)
	v_cvt_pk_bf16_f32 v64, v44, v45
	v_cvt_pk_bf16_f32 v65, v46, v47
	v_cvt_pk_bf16_f32 v66, v48, v49
	v_cvt_pk_bf16_f32 v67, v50, v51
	global_store_dwordx4 v18, v[64:67], s[16:17] nt
	s_xor_b32 s62, s62, 0x2000
	s_branch .Lcw1_loop
.Lcw1_last:
	s_waitcnt vmcnt(0)
	s_add_i32 s0, s19, s62
	v_add_u32_e32 v14, s0, v4
	v_add_u32_e32 v15, s0, v5
	v_add_u32_e32 v16, s0, v6
	v_add_u32_e32 v17, s0, v7
	ds_read2_b32 v[20:21], v14 offset0:0 offset1:32
	ds_read2_b32 v[22:23], v14 offset0:64 offset1:96
	ds_read2_b32 v[24:25], v14 offset0:128 offset1:160
	ds_read2_b32 v[26:27], v14 offset0:192 offset1:224
	ds_read2_b32 v[28:29], v15 offset0:0 offset1:32
	ds_read2_b32 v[30:31], v15 offset0:64 offset1:96
	ds_read2_b32 v[32:33], v15 offset0:128 offset1:160
	ds_read2_b32 v[34:35], v15 offset0:192 offset1:224
	ds_read2_b32 v[36:37], v16 offset0:0 offset1:32
	ds_read2_b32 v[38:39], v16 offset0:64 offset1:96
	ds_read2_b32 v[40:41], v16 offset0:128 offset1:160
	ds_read2_b32 v[42:43], v16 offset0:192 offset1:224
	ds_read2_b32 v[44:45], v17 offset0:0 offset1:32
	ds_read2_b32 v[46:47], v17 offset0:64 offset1:96
	ds_read2_b32 v[48:49], v17 offset0:128 offset1:160
	ds_read2_b32 v[50:51], v17 offset0:192 offset1:224
	v_mad_u32_u24 v18, v1, s18, v19
	s_lshl_b32 s1, s18, 3
	s_waitcnt lgkmcnt(12)
	v_cvt_pk_bf16_f32 v52, v20, v21
	v_cvt_pk_bf16_f32 v53, v22, v23
	v_cvt_pk_bf16_f32 v54, v24, v25
	v_cvt_pk_bf16_f32 v55, v26, v27
	global_store_dwordx4 v18, v[52:55], s[16:17] nt
	s_add_u32 s16, s16, s1
	s_addc_u32 s17, s17, 0
	s_waitcnt lgkmcnt(8)
	v_cvt_pk_bf16_f32 v56, v28, v29
	v_cvt_pk_bf16_f32 v57, v30, v31
	v_cvt_pk_bf16_f32 v58, v32, v33
	v_cvt_pk_bf16_f32 v59, v34, v35
	global_store_dwordx4 v18, v[56:59], s[16:17] nt
	s_add_u32 s16, s16, s1
	s_addc_u32 s17, s17, 0
	s_waitcnt lgkmcnt(4)
	v_cvt_pk_bf16_f32 v60, v36, v37
	v_cvt_pk_bf16_f32 v61, v38, v39
	v_cvt_pk_bf16_f32 v62, v40, v41
	v_cvt_pk_bf16_f32 v63, v42, v43
	global_store_dwordx4 v18, v[60:63], s[16:17] nt
	s_add_u32 s16, s16, s1
	s_addc_u32 s17, s17, 0
	s_waitcnt lgkmcnt(0)
	v_cvt_pk_bf16_f32 v64, v44, v45
	v_cvt_pk_bf16_f32 v65, v46, v47
	v_cvt_pk_bf16_f32 v66, v48, v49
	v_cvt_pk_bf16_f32 v67, v50, v51
	global_store_dwordx4 v18, v[64:67], s[16:17] nt
.Lcw1_end:
.LBB0_186:
	s_cmp_eq_u32 s100, 1
	s_cbranch_scc0 .Lp1_conv_skip
	s_mov_b32 s100, 2
	s_waitcnt lgkmcnt(0)
	s_barrier
	s_branch .Lp1_gemm_start
